# s_sleep 1 ahead of the exp block in mixer-B softmax sections (re-measure)
# speedup vs baseline: 1.0247x; 1.0247x over previous
; #define ATT_SBAR() __builtin_amdgcn_sched_barrier(0)
; #define ATT_PK4(P, BASE, OUT) do { u32x4 w = {cvtpk(P[BASE + 0], P[BASE + 1]), cvtpk(P[BASE + 2], P[BASE + 3]), cvtpk(P[BASE + 4], P[BASE + 5]), cvtpk(P[BASE + 6], P[BASE + 7])}; \
;     OUT = *reinterpret_cast<bf16x8*>(&w); } while (0)
; #define ATT_WRITE_K(so) do { *(bf16x8*)(K_lds + (so) + kswz<DQK>(kr, kc * 2)) = sk0; if constexpr (DQK == 128) *(bf16x8*)(K_lds + (so) + kswz<DQK>(32 + kr, kc * 2)) = sk1; } while (0)
; #define ATT_WRITE_V(so) do { *(bf16x8*)(V_lds + (so) + vst0) = sv0; *(bf16x8*)(V_lds + (so) + vst1) = sv1; } while (0)
; #define ATT_BAR() do { ATT_SBAR(); asm volatile("s_barrier" ::: "memory"); ATT_SBAR(); } while (0)
; #define ATT_VPAIR(buf, so, blk, ks) do { if constexpr (!(ABL & 8) && !(ABL & 32)) { buf[2 * (ks)] = vtr(vq0 + (so) + v_rd_off(blk, ks, 0)); buf[2 * (ks) + 1] = vtr(vq0 + (so) + v_rd_off(blk, ks, 1)); } } while (0)
; __device__ __forceinline__ void softmax_exp_pack(f32x16& p0, f32x16& p1, bf16x8& pa0, bf16x8& pa1, bf16x8& pa2, bf16x8& pa3) {
;     ...
;   for (int r = 0; r < 16; ++r) { p0[r] = __builtin_amdgcn_exp2f(p0[r]); p1[r] = __builtin_amdgcn_exp2f(p1[r]); }
;     ...
;   ATT_PK4(p0, 0, pa0); ATT_PK4(p0, 8, pa1); ATT_PK4(p1, 0, pa2); ATT_PK4(p1, 8, pa3);
;     ...
;     if constexpr (!(ABL & 4)) { ATT_WRITE_K(k2); ATT_WRITE_V(v1); }
;     ATT_SBAR();
; #pragma unroll
;     for (int ks = 0; ks < 4; ++ks) ATT_VPAIR(va, v0, 0, ks);
;     asm volatile("s_waitcnt lgkmcnt(8)" ::: "memory"); ATT_BAR();
.LBB0_283:
	s_sleep 1
	v_exp_f32_e32 v98, v98
	v_exp_f32_e32 v114, v114
	v_exp_f32_e32 v99, v99
	v_exp_f32_e32 v115, v115
	v_exp_f32_e32 v100, v100
	v_exp_f32_e32 v101, v101
	v_exp_f32_e32 v102, v102
	v_exp_f32_e32 v103, v103
	v_exp_f32_e32 v106, v106
	v_exp_f32_e32 v107, v107
	v_exp_f32_e32 v116, v116
	v_exp_f32_e32 v117, v117
	v_exp_f32_e32 v118, v118
	v_exp_f32_e32 v119, v119
	v_exp_f32_e32 v104, v104
	v_exp_f32_e32 v120, v120
	v_exp_f32_e32 v105, v105
	v_exp_f32_e32 v121, v121
	v_exp_f32_e32 v122, v122
	v_exp_f32_e32 v123, v123
	v_exp_f32_e32 v108, v108
	v_exp_f32_e32 v124, v124
	v_exp_f32_e32 v109, v109
	v_exp_f32_e32 v125, v125
	v_exp_f32_e32 v110, v110
	v_exp_f32_e32 v126, v126
	v_exp_f32_e32 v111, v111
	v_exp_f32_e32 v127, v127
	v_exp_f32_e32 v112, v112
	v_exp_f32_e32 v128, v128
	v_exp_f32_e32 v113, v113
	v_exp_f32_e32 v129, v129
	v_cvt_pk_bf16_f32 v2, v98, v99
	v_cvt_pk_bf16_f32 v3, v100, v101
	v_cvt_pk_bf16_f32 v4, v102, v103
	v_cvt_pk_bf16_f32 v6, v106, v107
	v_cvt_pk_bf16_f32 v10, v114, v115
	v_add_u32_e32 v114, s94, v169
	s_add_i32 s14, s95, 0
	s_waitcnt vmcnt(2)
	ds_write_b128 v114, v[224:227] offset:49152
	v_add_u32_e32 v114, s14, v167
	v_cvt_pk_bf16_f32 v5, v104, v105
	v_cvt_pk_bf16_f32 v7, v108, v109
	v_cvt_pk_bf16_f32 v8, v110, v111
	v_cvt_pk_bf16_f32 v9, v112, v113
	v_cvt_pk_bf16_f32 v11, v116, v117
	v_cvt_pk_bf16_f32 v12, v118, v119
	v_cvt_pk_bf16_f32 v13, v120, v121
	v_cvt_pk_bf16_f32 v14, v122, v123
	v_cvt_pk_bf16_f32 v15, v124, v125
	v_cvt_pk_bf16_f32 v16, v126, v127
	v_cvt_pk_bf16_f32 v17, v128, v129
	s_waitcnt vmcnt(1)
	ds_write_b128 v114, v[228:231]
	v_add_u32_e32 v114, s14, v168
	s_waitcnt vmcnt(0)
	ds_write_b128 v114, v[232:235]
	v_add_u32_e32 v249, s96, v172
	ds_read_b128 v[152:155], v249 offset:49152
	ds_read_b128 v[156:159], v249 offset:53760
	ds_read_b128 v[160:163], v249 offset:49184
	ds_read_b128 v[176:179], v249 offset:53792
	s_waitcnt lgkmcnt(4)
	s_barrier
; __device__ __forceinline__ float softmax_rowmax(const f32x16& p0, const f32x16& p1) {
;   const float m0 = p1[0] + 0.0f; float a, b;
;   asm("v_max3_f32 %0, %1, %2, %3\n\tv_max3_f32 %0, %0, %4, %5\n\tv_max3_f32 %0, %0, %6, %7\n\tv_max3_f32 %0, %0, %8, %9\n\t"
;       "v_max3_f32 %0, %0, %10, %11\n\tv_max3_f32 %0, %0, %12, %13\n\tv_max3_f32 %0, %0, %14, %15\n\tv_max3_f32 %0, %0, %16, %17"
;       : "=&v"(a) : "v"(m0), "v"(p0[0]), "v"(p0[1]), "v"(p0[2]), "v"(p0[3]), "v"(p0[4]), "v"(p0[5]), "v"(p0[6]), "v"(p0[7]), "v"(p0[8]), "v"(p0[9]), "v"(p0[10]), "v"(p0[11]), "v"(p0[12]), "v"(p0[13]), "v"(p0[14]), "v"(p0[15]));
;   asm("v_max3_f32 %0, %1, %2, %3\n\tv_max3_f32 %0, %0, %4, %5\n\tv_max3_f32 %0, %0, %6, %7\n\tv_max3_f32 %0, %0, %8, %9\n\t"
;       "v_max3_f32 %0, %0, %10, %11\n\tv_max3_f32 %0, %0, %12, %13\n\tv_max3_f32 %0, %0, %14, %15\n\tv_max_f32 %0, %0, %16"
;       : "=&v"(b) : "v"(a), "v"(p1[1]), "v"(p1[2]), "v"(p1[3]), "v"(p1[4]), "v"(p1[5]), "v"(p1[6]), "v"(p1[7]), "v"(p1[8]), "v"(p1[9]), "v"(p1[10]), "v"(p1[11]), "v"(p1[12]), "v"(p1[13]), "v"(p1[14]), "v"(p1[15]));
;   return b;
	s_setprio 2
	s_waitcnt lgkmcnt(3)
	v_mfma_f32_32x32x16_bf16 v[98:113], v[152:155], v[136:139], v[82:97]
	ds_read_b128 v[180:183], v249 offset:49216
	s_waitcnt lgkmcnt(3)
	v_mfma_f32_32x32x16_bf16 v[114:129], v[156:159], v[136:139], v[82:97]
	ds_read_b128 v[186:189], v249 offset:53824
	v_add_u32_e32 v248, s37, v131
	s_waitcnt lgkmcnt(3)
	v_mfma_f32_32x32x16_bf16 v[98:113], v[160:163], v[140:143], v[98:113]
	ds_read_b128 v[190:193], v249 offset:49248
	ds_read_b64_tr_b16 v[198:199], v248
	ds_read_b64_tr_b16 v[200:201], v248 offset:2048
	s_waitcnt lgkmcnt(5)
	v_mfma_f32_32x32x16_bf16 v[114:129], v[176:179], v[140:143], v[114:129]
	ds_read_b128 v[194:197], v249 offset:53856
	ds_read_b64_tr_b16 v[212:213], v248 offset:4096
	ds_read_b64_tr_b16 v[214:215], v248 offset:6144
	s_waitcnt lgkmcnt(7)
	v_mfma_f32_32x32x16_bf16 v[98:113], v[180:183], v[144:147], v[98:113]
	ds_read_b64_tr_b16 v[216:217], v248 offset:8192
	ds_read_b64_tr_b16 v[218:219], v248 offset:10240
	s_waitcnt lgkmcnt(8)
	v_mfma_f32_32x32x16_bf16 v[114:129], v[186:189], v[144:147], v[114:129]
	ds_read_b64_tr_b16 v[220:221], v248 offset:12288
	ds_read_b64_tr_b16 v[222:223], v248 offset:14336
	s_waitcnt lgkmcnt(9)
	v_mfma_f32_32x32x16_bf16 v[98:113], v[190:193], v[148:151], v[98:113]
	s_waitcnt lgkmcnt(6)
	v_mfma_f32_32x32x16_bf16 v[114:129], v[194:197], v[148:151], v[114:129]
	v_mfma_f32_32x32x16_bf16 v[18:33], v[2:5], v[198:201], v[18:33]
	ds_read_b64_tr_b16 v[236:237], v248 offset:512
	ds_read_b64_tr_b16 v[238:239], v248 offset:2560
	s_waitcnt lgkmcnt(6)
	v_mfma_f32_32x32x16_bf16 v[18:33], v[6:9], v[212:215], v[18:33]
	ds_read_b64_tr_b16 v[198:199], v248 offset:4608
	ds_read_b64_tr_b16 v[200:201], v248 offset:6656
	s_waitcnt lgkmcnt(6)
	v_mfma_f32_32x32x16_bf16 v[18:33], v[10:13], v[216:219], v[18:33]
	ds_read_b64_tr_b16 v[212:213], v248 offset:8704
	ds_read_b64_tr_b16 v[214:215], v248 offset:10752
	s_waitcnt lgkmcnt(6)
	v_mfma_f32_32x32x16_bf16 v[18:33], v[14:17], v[220:223], v[18:33]
	ds_read_b64_tr_b16 v[216:217], v248 offset:12800
	ds_read_b64_tr_b16 v[218:219], v248 offset:14848
	v_max3_f32 v249, v98, v99, v100
	s_waitcnt lgkmcnt(6)
	v_mfma_f32_32x32x16_bf16 v[34:49], v[2:5], v[236:239], v[34:49]
	ds_read_b64_tr_b16 v[220:221], v248 offset:1024
	ds_read_b64_tr_b16 v[222:223], v248 offset:3072
	v_max3_f32 v173, v114, v115, v116
	s_waitcnt lgkmcnt(6)
	v_mfma_f32_32x32x16_bf16 v[34:49], v[6:9], v[198:201], v[34:49]
	ds_read_b64_tr_b16 v[236:237], v248 offset:5120
	ds_read_b64_tr_b16 v[238:239], v248 offset:7168
	v_max3_f32 v249, v249, v101, v102
	s_waitcnt lgkmcnt(6)
	v_mfma_f32_32x32x16_bf16 v[34:49], v[10:13], v[212:215], v[34:49]
	ds_read_b64_tr_b16 v[198:199], v248 offset:9216
	ds_read_b64_tr_b16 v[200:201], v248 offset:11264
	v_max3_f32 v173, v173, v117, v118
	s_waitcnt lgkmcnt(6)
	v_mfma_f32_32x32x16_bf16 v[34:49], v[14:17], v[216:219], v[34:49]
	ds_read_b64_tr_b16 v[212:213], v248 offset:13312
	ds_read_b64_tr_b16 v[214:215], v248 offset:15360
	v_max3_f32 v249, v249, v103, v104
	s_waitcnt lgkmcnt(6)
	v_mfma_f32_32x32x16_bf16 v[50:65], v[2:5], v[220:223], v[50:65]
	ds_read_b64_tr_b16 v[216:217], v248 offset:1536
	ds_read_b64_tr_b16 v[218:219], v248 offset:3584
	v_max3_f32 v173, v173, v119, v120
	s_waitcnt lgkmcnt(6)
	v_mfma_f32_32x32x16_bf16 v[50:65], v[6:9], v[236:239], v[50:65]
	ds_read_b64_tr_b16 v[220:221], v248 offset:5632
	ds_read_b64_tr_b16 v[222:223], v248 offset:7680
	v_max3_f32 v249, v249, v105, v106
	s_waitcnt lgkmcnt(6)
	v_mfma_f32_32x32x16_bf16 v[50:65], v[10:13], v[198:201], v[50:65]
	ds_read_b64_tr_b16 v[236:237], v248 offset:9728
	ds_read_b64_tr_b16 v[238:239], v248 offset:11776
	v_max3_f32 v173, v173, v121, v122
	s_waitcnt lgkmcnt(6)
	v_mfma_f32_32x32x16_bf16 v[50:65], v[14:17], v[212:215], v[50:65]
	ds_read_b64_tr_b16 v[198:199], v248 offset:13824
	ds_read_b64_tr_b16 v[200:201], v248 offset:15872
	v_max3_f32 v249, v249, v107, v108
	s_waitcnt lgkmcnt(6)
	v_mfma_f32_32x32x16_bf16 v[66:81], v[2:5], v[216:219], v[66:81]
	v_max3_f32 v173, v173, v123, v124
	s_min_u32 s14, s97, 0x7c
	s_lshl_b32 s14, s14, 17
	s_add_i32 s14, s14, 0x60000
	buffer_load_dwordx4 v[224:227], v170, s[8:11], s14 offen
	s_waitcnt lgkmcnt(4)
	v_mfma_f32_32x32x16_bf16 v[66:81], v[6:9], v[220:223], v[66:81]
	v_max3_f32 v249, v249, v109, v110
	s_add_i32 s19, s36, 0xffff0000
	s_mov_b32 s14, s10
	s_mov_b32 s15, s11
	buffer_load_dwordx4 v[228:231], v171, s[12:15], s19 offen
	s_waitcnt lgkmcnt(2)
	v_mfma_f32_32x32x16_bf16 v[66:81], v[10:13], v[236:239], v[66:81]
	v_max3_f32 v173, v173, v125, v126
	buffer_load_dwordx4 v[232:235], v171, s[12:15], s36 offen
	s_waitcnt lgkmcnt(0)
	v_mfma_f32_32x32x16_bf16 v[66:81], v[14:17], v[198:201], v[66:81]
	v_max3_f32 v249, v249, v111, v112
	v_mfma_f32_4x4x4_16b_bf16 v[240:243], v[2:3], v[132:133], v[240:243]
	v_max3_f32 v173, v173, v127, v128
	v_mfma_f32_4x4x4_16b_bf16 v[244:247], v[4:5], v[132:133], v[244:247]
	v_mfma_f32_4x4x4_16b_bf16 v[240:243], v[6:7], v[132:133], v[240:243]
	v_max_f32 v249, v249, v113
	v_mfma_f32_4x4x4_16b_bf16 v[244:247], v[8:9], v[132:133], v[244:247]
	v_mfma_f32_4x4x4_16b_bf16 v[240:243], v[10:11], v[132:133], v[240:243]
	v_max_f32 v173, v173, v129
	v_mfma_f32_4x4x4_16b_bf16 v[244:247], v[12:13], v[132:133], v[244:247]
	v_mfma_f32_4x4x4_16b_bf16 v[240:243], v[14:15], v[132:133], v[240:243]
	v_max_f32 v173, v173, v249
	v_mfma_f32_4x4x4_16b_bf16 v[244:247], v[16:17], v[132:133], v[244:247]
	s_setprio 0
	s_barrier
	s_add_i32 s36, s36, 0x20000
	s_add_i32 s97, s97, 1
	s_cmpk_eq_i32 s97, 0x7e
	s_cbranch_scc1 .LBB0_290
	s_mov_b32 s14, s94
	s_mov_b32 s94, s18
	s_mov_b32 s18, s96
	s_mov_b32 s15, s95
	s_mov_b32 s95, s93
	s_mov_b32 s93, s37
	s_branch .LBB0_282

; #define ATT_SBAR() __builtin_amdgcn_sched_barrier(0)
; #define ATT_PK4(P, BASE, OUT) do { u32x4 w = {cvtpk(P[BASE + 0], P[BASE + 1]), cvtpk(P[BASE + 2], P[BASE + 3]), cvtpk(P[BASE + 4], P[BASE + 5]), cvtpk(P[BASE + 6], P[BASE + 7])}; \
;     OUT = *reinterpret_cast<bf16x8*>(&w); } while (0)
; #define ATT_WRITE_K(so) do { *(bf16x8*)(K_lds + (so) + kswz<DQK>(kr, kc * 2)) = sk0; if constexpr (DQK == 128) *(bf16x8*)(K_lds + (so) + kswz<DQK>(32 + kr, kc * 2)) = sk1; } while (0)
; #define ATT_WRITE_V(so) do { *(bf16x8*)(V_lds + (so) + vst0) = sv0; *(bf16x8*)(V_lds + (so) + vst1) = sv1; } while (0)
; #define ATT_BAR() do { ATT_SBAR(); asm volatile("s_barrier" ::: "memory"); ATT_SBAR(); } while (0)
; #define ATT_VPAIR(buf, so, blk, ks) do { if constexpr (!(ABL & 8) && !(ABL & 32)) { buf[2 * (ks)] = vtr(vq0 + (so) + v_rd_off(blk, ks, 0)); buf[2 * (ks) + 1] = vtr(vq0 + (so) + v_rd_off(blk, ks, 1)); } } while (0)
; __device__ __forceinline__ void softmax_exp_pack(f32x16& p0, f32x16& p1, bf16x8& pa0, bf16x8& pa1, bf16x8& pa2, bf16x8& pa3) {
;     ...
;   for (int r = 0; r < 16; ++r) { p0[r] = __builtin_amdgcn_exp2f(p0[r]); p1[r] = __builtin_amdgcn_exp2f(p1[r]); }
;     ...
;   ATT_PK4(p0, 0, pa0); ATT_PK4(p0, 8, pa1); ATT_PK4(p1, 0, pa2); ATT_PK4(p1, 8, pa3);
;     ...
;     if constexpr (!(ABL & 4)) { ATT_WRITE_K(k2); ATT_WRITE_V(v1); }
;     ATT_SBAR();
; #pragma unroll
;     for (int ks = 0; ks < 4; ++ks) ATT_VPAIR(va, v0, 0, ks);
;     asm volatile("s_waitcnt lgkmcnt(8)" ::: "memory"); ATT_BAR();
.LBB0_298:
	s_sleep 1
	v_exp_f32_e32 v98, v98
	v_exp_f32_e32 v114, v114
	v_exp_f32_e32 v99, v99
	v_exp_f32_e32 v115, v115
	v_exp_f32_e32 v100, v100
	v_exp_f32_e32 v101, v101
	v_exp_f32_e32 v102, v102
	v_exp_f32_e32 v103, v103
	v_exp_f32_e32 v106, v106
	v_exp_f32_e32 v107, v107
	v_exp_f32_e32 v116, v116
	v_exp_f32_e32 v117, v117
	v_exp_f32_e32 v118, v118
	v_exp_f32_e32 v119, v119
	v_exp_f32_e32 v104, v104
	v_exp_f32_e32 v120, v120
	v_exp_f32_e32 v105, v105
	v_exp_f32_e32 v121, v121
	v_exp_f32_e32 v122, v122
	v_exp_f32_e32 v123, v123
	v_exp_f32_e32 v108, v108
	v_exp_f32_e32 v124, v124
	v_exp_f32_e32 v109, v109
	v_exp_f32_e32 v125, v125
	v_exp_f32_e32 v110, v110
	v_exp_f32_e32 v126, v126
	v_exp_f32_e32 v111, v111
	v_exp_f32_e32 v127, v127
	v_exp_f32_e32 v112, v112
	v_exp_f32_e32 v128, v128
	v_exp_f32_e32 v113, v113
	v_exp_f32_e32 v129, v129
	v_cvt_pk_bf16_f32 v18, v98, v99
	v_cvt_pk_bf16_f32 v19, v100, v101
	v_cvt_pk_bf16_f32 v20, v102, v103
	v_cvt_pk_bf16_f32 v22, v106, v107
	v_cvt_pk_bf16_f32 v26, v114, v115
	v_add_u32_e32 v114, s49, v170
	s_add_i32 s14, s50, 0
	s_waitcnt vmcnt(2)
	ds_write_b128 v114, v[224:227] offset:49152
	v_add_u32_e32 v114, s14, v168
	v_cvt_pk_bf16_f32 v21, v104, v105
	v_cvt_pk_bf16_f32 v23, v108, v109
	v_cvt_pk_bf16_f32 v24, v110, v111
	v_cvt_pk_bf16_f32 v25, v112, v113
	v_cvt_pk_bf16_f32 v27, v116, v117
	v_cvt_pk_bf16_f32 v28, v118, v119
	v_cvt_pk_bf16_f32 v29, v120, v121
	v_cvt_pk_bf16_f32 v30, v122, v123
	v_cvt_pk_bf16_f32 v31, v124, v125
	v_cvt_pk_bf16_f32 v32, v126, v127
	v_cvt_pk_bf16_f32 v33, v128, v129
	s_waitcnt vmcnt(1)
	ds_write_b128 v114, v[228:231]
	v_add_u32_e32 v114, s14, v169
	s_waitcnt vmcnt(0)
	ds_write_b128 v114, v[232:235]
	v_add_u32_e32 v249, s18, v173
	ds_read_b128 v[152:155], v249 offset:49152
	ds_read_b128 v[156:159], v249 offset:53760
	ds_read_b128 v[160:163], v249 offset:49184
	ds_read_b128 v[176:179], v249 offset:53792
	s_waitcnt lgkmcnt(4)
	s_barrier
; __device__ __forceinline__ float softmax_rowmax(const f32x16& p0, const f32x16& p1) {
;   const float m0 = p1[0] + 0.0f; float a, b;
;   asm("v_max3_f32 %0, %1, %2, %3\n\tv_max3_f32 %0, %0, %4, %5\n\tv_max3_f32 %0, %0, %6, %7\n\tv_max3_f32 %0, %0, %8, %9\n\t"
;       "v_max3_f32 %0, %0, %10, %11\n\tv_max3_f32 %0, %0, %12, %13\n\tv_max3_f32 %0, %0, %14, %15\n\tv_max3_f32 %0, %0, %16, %17"
;       : "=&v"(a) : "v"(m0), "v"(p0[0]), "v"(p0[1]), "v"(p0[2]), "v"(p0[3]), "v"(p0[4]), "v"(p0[5]), "v"(p0[6]), "v"(p0[7]), "v"(p0[8]), "v"(p0[9]), "v"(p0[10]), "v"(p0[11]), "v"(p0[12]), "v"(p0[13]), "v"(p0[14]), "v"(p0[15]));
;   asm("v_max3_f32 %0, %1, %2, %3\n\tv_max3_f32 %0, %0, %4, %5\n\tv_max3_f32 %0, %0, %6, %7\n\tv_max3_f32 %0, %0, %8, %9\n\t"
;       "v_max3_f32 %0, %0, %10, %11\n\tv_max3_f32 %0, %0, %12, %13\n\tv_max3_f32 %0, %0, %14, %15\n\tv_max_f32 %0, %0, %16"
;       : "=&v"(b) : "v"(a), "v"(p1[1]), "v"(p1[2]), "v"(p1[3]), "v"(p1[4]), "v"(p1[5]), "v"(p1[6]), "v"(p1[7]), "v"(p1[8]), "v"(p1[9]), "v"(p1[10]), "v"(p1[11]), "v"(p1[12]), "v"(p1[13]), "v"(p1[14]), "v"(p1[15]));
;   return b;
	s_setprio 2
	s_waitcnt lgkmcnt(3)
	v_mfma_f32_32x32x16_bf16 v[98:113], v[152:155], v[136:139], v[82:97]
	ds_read_b128 v[180:183], v249 offset:49216
	s_waitcnt lgkmcnt(3)
	v_mfma_f32_32x32x16_bf16 v[114:129], v[156:159], v[136:139], v[82:97]
	ds_read_b128 v[186:189], v249 offset:53824
	v_add_u32_e32 v248, s37, v131
	s_waitcnt lgkmcnt(3)
	v_mfma_f32_32x32x16_bf16 v[98:113], v[160:163], v[140:143], v[98:113]
	ds_read_b128 v[190:193], v249 offset:49248
	ds_read_b64_tr_b16 v[198:199], v248
	ds_read_b64_tr_b16 v[200:201], v248 offset:2048
	s_waitcnt lgkmcnt(5)
	v_mfma_f32_32x32x16_bf16 v[114:129], v[176:179], v[140:143], v[114:129]
	ds_read_b128 v[194:197], v249 offset:53856
	ds_read_b64_tr_b16 v[212:213], v248 offset:4096
	ds_read_b64_tr_b16 v[214:215], v248 offset:6144
	s_waitcnt lgkmcnt(7)
	v_mfma_f32_32x32x16_bf16 v[98:113], v[180:183], v[144:147], v[98:113]
	ds_read_b64_tr_b16 v[216:217], v248 offset:8192
	ds_read_b64_tr_b16 v[218:219], v248 offset:10240
	s_waitcnt lgkmcnt(8)
	v_mfma_f32_32x32x16_bf16 v[114:129], v[186:189], v[144:147], v[114:129]
	ds_read_b64_tr_b16 v[220:221], v248 offset:12288
	ds_read_b64_tr_b16 v[222:223], v248 offset:14336
	s_waitcnt lgkmcnt(9)
	v_mfma_f32_32x32x16_bf16 v[98:113], v[190:193], v[148:151], v[98:113]
	s_waitcnt lgkmcnt(6)
	v_mfma_f32_32x32x16_bf16 v[114:129], v[194:197], v[148:151], v[114:129]
	v_mfma_f32_32x32x16_bf16 v[66:81], v[18:21], v[198:201], v[66:81]
	ds_read_b64_tr_b16 v[236:237], v248 offset:512
	ds_read_b64_tr_b16 v[238:239], v248 offset:2560
	s_waitcnt lgkmcnt(6)
	v_mfma_f32_32x32x16_bf16 v[66:81], v[22:25], v[212:215], v[66:81]
	ds_read_b64_tr_b16 v[198:199], v248 offset:4608
	ds_read_b64_tr_b16 v[200:201], v248 offset:6656
	s_waitcnt lgkmcnt(6)
	v_mfma_f32_32x32x16_bf16 v[66:81], v[26:29], v[216:219], v[66:81]
	ds_read_b64_tr_b16 v[212:213], v248 offset:8704
	ds_read_b64_tr_b16 v[214:215], v248 offset:10752
	s_waitcnt lgkmcnt(6)
	v_mfma_f32_32x32x16_bf16 v[66:81], v[30:33], v[220:223], v[66:81]
	ds_read_b64_tr_b16 v[216:217], v248 offset:12800
	ds_read_b64_tr_b16 v[218:219], v248 offset:14848
	v_max3_f32 v249, v98, v99, v100
	s_waitcnt lgkmcnt(6)
	v_mfma_f32_32x32x16_bf16 v[50:65], v[18:21], v[236:239], v[50:65]
	ds_read_b64_tr_b16 v[220:221], v248 offset:1024
	ds_read_b64_tr_b16 v[222:223], v248 offset:3072
	v_max3_f32 v174, v114, v115, v116
	s_waitcnt lgkmcnt(6)
	v_mfma_f32_32x32x16_bf16 v[50:65], v[22:25], v[198:201], v[50:65]
	ds_read_b64_tr_b16 v[236:237], v248 offset:5120
	ds_read_b64_tr_b16 v[238:239], v248 offset:7168
	v_max3_f32 v249, v249, v101, v102
	s_waitcnt lgkmcnt(6)
	v_mfma_f32_32x32x16_bf16 v[50:65], v[26:29], v[212:215], v[50:65]
	ds_read_b64_tr_b16 v[198:199], v248 offset:9216
	ds_read_b64_tr_b16 v[200:201], v248 offset:11264
	v_max3_f32 v174, v174, v117, v118
	s_waitcnt lgkmcnt(6)
	v_mfma_f32_32x32x16_bf16 v[50:65], v[30:33], v[216:219], v[50:65]
	ds_read_b64_tr_b16 v[212:213], v248 offset:13312
	ds_read_b64_tr_b16 v[214:215], v248 offset:15360
	v_max3_f32 v249, v249, v103, v104
	s_waitcnt lgkmcnt(6)
	v_mfma_f32_32x32x16_bf16 v[34:49], v[18:21], v[220:223], v[34:49]
	ds_read_b64_tr_b16 v[216:217], v248 offset:1536
	ds_read_b64_tr_b16 v[218:219], v248 offset:3584
	v_max3_f32 v174, v174, v119, v120
	s_waitcnt lgkmcnt(6)
	v_mfma_f32_32x32x16_bf16 v[34:49], v[22:25], v[236:239], v[34:49]
	ds_read_b64_tr_b16 v[220:221], v248 offset:5632
	ds_read_b64_tr_b16 v[222:223], v248 offset:7680
	v_max3_f32 v249, v249, v105, v106
	s_waitcnt lgkmcnt(6)
	v_mfma_f32_32x32x16_bf16 v[34:49], v[26:29], v[198:201], v[34:49]
	ds_read_b64_tr_b16 v[236:237], v248 offset:9728
	ds_read_b64_tr_b16 v[238:239], v248 offset:11776
	v_max3_f32 v174, v174, v121, v122
	s_waitcnt lgkmcnt(6)
	v_mfma_f32_32x32x16_bf16 v[34:49], v[30:33], v[212:215], v[34:49]
	ds_read_b64_tr_b16 v[198:199], v248 offset:13824
	ds_read_b64_tr_b16 v[200:201], v248 offset:15872
	v_max3_f32 v249, v249, v107, v108
	s_waitcnt lgkmcnt(6)
	v_mfma_f32_32x32x16_bf16 v[2:17], v[18:21], v[216:219], v[2:17]
	v_max3_f32 v174, v174, v123, v124
	s_min_u32 s14, s90, 0x7c
	s_lshl_b32 s14, s14, 17
	s_add_i32 s19, s14, 0x60000
	s_add_i32 s92, s36, 0xffff0000
	s_mov_b32 s14, s10
	s_mov_b32 s15, s11
	buffer_load_dwordx4 v[224:227], v171, s[8:11], s19 offen
	s_waitcnt lgkmcnt(4)
	v_mfma_f32_32x32x16_bf16 v[2:17], v[22:25], v[220:223], v[2:17]
	v_max3_f32 v249, v249, v109, v110
	buffer_load_dwordx4 v[228:231], v172, s[12:15], s92 offen
	s_waitcnt lgkmcnt(2)
	v_mfma_f32_32x32x16_bf16 v[2:17], v[26:29], v[236:239], v[2:17]
	v_max3_f32 v174, v174, v125, v126
	buffer_load_dwordx4 v[232:235], v172, s[12:15], s36 offen
	s_waitcnt lgkmcnt(0)
	v_mfma_f32_32x32x16_bf16 v[2:17], v[30:33], v[198:201], v[2:17]
	v_max3_f32 v249, v249, v111, v112
	v_mfma_f32_4x4x4_16b_bf16 v[240:243], v[18:19], v[132:133], v[240:243]
	v_max3_f32 v174, v174, v127, v128
	v_mfma_f32_4x4x4_16b_bf16 v[244:247], v[20:21], v[132:133], v[244:247]
	v_mfma_f32_4x4x4_16b_bf16 v[240:243], v[22:23], v[132:133], v[240:243]
	v_max_f32 v249, v249, v113
	v_mfma_f32_4x4x4_16b_bf16 v[244:247], v[24:25], v[132:133], v[244:247]
	v_mfma_f32_4x4x4_16b_bf16 v[240:243], v[26:27], v[132:133], v[240:243]
	v_max_f32 v174, v174, v129
	v_mfma_f32_4x4x4_16b_bf16 v[244:247], v[28:29], v[132:133], v[244:247]
	v_mfma_f32_4x4x4_16b_bf16 v[240:243], v[30:31], v[132:133], v[240:243]
	v_max_f32 v174, v174, v249
	v_mfma_f32_4x4x4_16b_bf16 v[244:247], v[32:33], v[132:133], v[244:247]
	s_setprio 0
	s_barrier
	s_add_i32 s36, s36, 0x20000
	s_add_i32 s90, s90, 1
	s_cmpk_eq_i32 s90, 0x7e
	s_cbranch_scc1 .LBB0_305
	s_mov_b32 s14, s49
	s_mov_b32 s49, s51
	s_mov_b32 s51, s18
	s_mov_b32 s15, s50
	s_mov_b32 s50, s48
	s_mov_b32 s48, s37
	s_branch .LBB0_297
